# input projection: six unit-index exchanges (no workgroup with three forget-gate tiles) combined with one more weight-conversion item per wave moved to the top-k phase
# baseline (speedup 1.0000x reference)
.LBB0_265:
	v_readlane_b32 s12, v235, 0
	v_readlane_b32 s14, v235, 2
	s_cmp_lt_i32 s16, s27
	s_cselect_b64 s[8:9], -1, 0
	s_cmp_eq_u32 s27, s14
	v_readlane_b32 s13, v235, 1
	s_cselect_b64 s[2:3], -1, 0
	s_cmp_lg_u32 s27, s14
	s_cselect_b64 s[12:13], -1, 0
	s_and_b64 s[8:9], s[8:9], s[12:13]
	s_mul_i32 s52, s14, 0xffffffe0
	s_and_b64 vcc, exec, s[8:9]
	v_readlane_b32 s15, v235, 3
	s_cbranch_vccnz .LBB0_293
	s_add_i32 s8, s52, 0x8800
	s_and_b64 s[0:1], s[0:1], exec
	s_cselect_b32 s53, s8, 0x8400
	s_and_b64 s[0:1], s[2:3], exec
	v_readlane_b32 s0, v235, 16
	s_cselect_b32 s34, 0, s27
	v_readlane_b32 s1, v235, 17
	v_mov_b32_e32 v64, v186
	s_sub_i32 s0, s0, s34
	s_lshl_b32 s0, s0, 3
	v_readfirstlane_b32 s1, v64
	s_ashr_i32 s35, s1, 6
	s_add_i32 s16, s35, s0
	s_cmp_ge_i32 s16, s53
	s_cbranch_scc1 .LBB0_293
	s_mul_hi_i32 s12, s16, 0x3e0f83e1
	s_lshr_b32 s13, s12, 31
	s_ashr_i32 s22, s12, 9
	s_add_i32 s22, s22, s13
	s_mul_i32 s12, s22, 0xfffff7c0
	s_add_i32 s17, s12, s16
	s_add_i32 s12, s17, 0xfffffd40
	s_cmpk_lt_u32 s12, 0x2c0
	s_cselect_b64 s[12:13], -1, 0
	s_and_b64 s[14:15], s[12:13], exec
	s_load_dwordx4 s[0:3], s[10:11], 0x70
	s_load_dwordx2 s[8:9], s[10:11], 0x80
	s_cselect_b32 s18, 0xfffffd40, 0
	s_cmpk_lt_i32 s17, 0x580
	s_cselect_b64 s[14:15], -1, 0
	s_and_b64 vcc, exec, s[14:15]
	s_cselect_b32 s20, s18, 0xfffffa80
	s_add_i32 s20, s20, s17
	s_cbranch_vccnz .LBB0_269
	s_and_b32 s30, s16, 31
	s_ashr_i32 s31, s20, 5
	s_waitcnt lgkmcnt(0)
	s_mov_b64 s[16:17], s[8:9]
	s_load_dwordx2 s[10:11], s[10:11], 0x98
	s_cbranch_execz .LBB0_270
	s_branch .LBB0_271

.LBB0_712:
	s_or_b64 exec, exec, s[0:1]
	v_readlane_b32 s0, v235, 0
	v_readlane_b32 s2, v235, 2
	v_readlane_b32 s3, v235, 3
	v_readlane_b32 s1, v235, 1
	s_cmp_gt_i32 s2, 63
	v_readlane_b32 s2, v235, 16
	s_cselect_b64 s[0:1], -1, 0
	s_cmp_lt_i32 s2, 32
	v_readlane_b32 s3, v235, 17
	s_cselect_b64 s[4:5], -1, 0
	s_cmp_gt_i32 s2, 31
	s_cselect_b64 s[2:3], -1, 0
	s_and_b64 s[2:3], s[2:3], s[0:1]
	s_mov_b64 s[6:7], s[46:47]
	s_mov_b64 s[0:1], -1
	s_and_b64 vcc, exec, s[2:3]
	v_readlane_b32 s46, v235, 10
	s_waitcnt lgkmcnt(0)
	s_barrier
	v_readlane_b32 s47, v235, 11
	s_cbranch_vccz .LBB0_724
	v_readlane_b32 s0, v235, 12
	v_readlane_b32 s1, v235, 13
	v_mov_b32_e32 v0, v186
	s_add_i32 s0, s52, s0
	v_readfirstlane_b32 s1, v0
	s_ashr_i32 s12, s1, 6
	s_add_i32 s0, s0, s12
	s_add_i32 s30, s0, 0x8700
	s_cmp_gt_i32 s30, 0x83ff
	s_cbranch_scc1 .LBB0_723
	s_load_dwordx4 s[0:3], s[6:7], 0x70
	s_load_dwordx2 s[8:9], s[6:7], 0x80
	s_load_dwordx2 s[10:11], s[6:7], 0x98
	s_mulk_i32 s12, 0x2100
	v_bfe_u32 v12, v0, 1, 5
	v_lshlrev_b32_e32 v1, 2, v0
	v_bfe_u32 v14, v0, 3, 3
	v_and_b32_e32 v0, 7, v0
	s_add_i32 s12, s12, 0
	v_and_b32_e32 v2, 28, v1
	v_mul_u32_u24_e32 v1, 0x220, v0
	v_lshlrev_b32_e32 v3, 2, v14
	v_lshlrev_b32_e32 v8, 4, v0
	v_add3_u32 v15, s12, v1, v3
	v_add_u32_e32 v0, s12, v8
	v_mul_u32_u24_e32 v1, 0x88, v14
	v_mov_b32_e32 v9, 0
	v_add_u32_e32 v20, v0, v1
	s_add_i32 s31, s46, 0xffffff00
	s_mov_b32 s13, 0
	v_and_b32_e32 v13, 28, v12
	v_or_b32_e32 v16, 8, v14
	v_or_b32_e32 v17, 16, v14
	v_or_b32_e32 v18, 24, v14
	v_lshlrev_b32_e32 v10, 2, v2
	v_mov_b32_e32 v11, v9
	s_mov_b32 s33, 0xc3e00000
	v_mov_b32_e32 v19, 0x43e00000
	v_add_u32_e32 v21, 0x880, v20
	v_add_u32_e32 v22, 0xcc0, v20
	s_branch .LBB0_717
